# v042
# speedup vs baseline: 1.1423x; 1.0623x over previous
.Ltok_done:
	v_cmp_ne_u32_e32 vcc, 0, v7
	s_and_saveexec_b64 s[6:7], vcc
	v_mov_b32_e32 v1, 1
	v_mov_b32_e32 v2, 0
	ds_write_b32 v2, v1 offset:24832
	s_or_b64 exec, exec, s[6:7]
	s_mov_b32 s5, 0
	s_cmp_eq_u32 s16, 0
	s_cselect_b64 vcc, -1, 0
	v_mov_b32_e32 v157, 0
	s_waitcnt lgkmcnt(0)
	s_barrier
	ds_read_b32 v1, v157 offset:24832
	v_lshrrev_b32_e32 v108, 6, v0
	v_and_b32_e32 v4, 63, v0
	s_movk_i32 s0, 0x1000
	v_mov_b32_e32 v9, v157
	s_waitcnt lgkmcnt(0)
	v_readfirstlane_b32 s4, v1
	v_lshl_or_b32 v1, s16, 3, v108
	v_mul_u32_u24_e32 v1, 0x300, v1
	v_lshlrev_b32_e32 v156, 4, v1
	v_lshl_add_u64 v[2:3], s[8:9], 0, v[156:157]
	v_lshlrev_b32_e32 v156, 4, v4
	v_lshl_add_u64 v[2:3], v[2:3], 0, v[156:157]
	v_add_co_u32_e64 v4, s[0:1], s0, v2
	v_lshl_or_b32 v1, s16, 4, v108
	s_nop 0
	v_addc_co_u32_e64 v5, s[0:1], 0, v3, s[0:1]
	s_movk_i32 s0, 0x2000
	s_nop 0
	v_add_co_u32_e64 v6, s[0:1], s0, v2
	v_or_b32_e32 v8, 8, v1
	s_nop 0
	v_addc_co_u32_e64 v7, s[0:1], 0, v3, s[0:1]
	s_add_u32 s0, s8, 0x30000
	v_mul_u32_u24_e32 v8, 0xc0, v8
	s_addc_u32 s1, s9, 0
	v_lshlrev_b32_e32 v8, 4, v8
	v_mul_u32_u24_e32 v1, 0xc0, v1
	v_lshl_add_u64 v[92:93], s[0:1], 0, v[8:9]
	v_lshlrev_b32_e32 v8, 4, v1
	s_cmp_lg_u32 s4, 0
	v_lshl_add_u64 v[8:9], s[0:1], 0, v[8:9]
	s_cselect_b64 s[12:13], -1, 0
	s_lshl_b32 s0, s16, 11
	s_add_u32 s0, s8, s0
	s_addc_u32 s1, s9, 0
	v_and_b32_e32 v10, 0x1c0, v0
	v_mov_b32_e32 v11, v157
	v_lshl_add_u64 v[10:11], s[0:1], 0, v[10:11]
	v_and_b32_e32 v12, 48, v0
	v_mov_b32_e32 v13, v157
	v_and_b32_e32 v161, 15, v0
	v_lshl_add_u64 v[10:11], v[10:11], 0, v[12:13]
	s_mov_b64 s[0:1], 0x48000
	v_lshrrev_b32_e32 v12, 5, v0
	v_bfe_u32 v13, v0, 5, 1
	v_bfe_u32 v109, v0, 4, 2
	v_lshl_add_u64 v[72:73], v[10:11], 0, s[0:1]
	s_mov_b32 s0, 0x48000
	v_lshlrev_b32_e32 v1, 3, v0
	v_and_or_b32 v12, v12, 2, v13
	v_lshlrev_b32_e32 v13, 4, v161
	v_lshrrev_b32_e32 v0, 1, v0
	v_add_co_u32_e64 v10, s[0:1], s0, v10
	v_and_b32_e32 v1, 0xc00, v1
	v_lshl_or_b32 v12, v12, 8, v13
	v_and_b32_e32 v0, 8, v0
	v_lshl_add_u64 v[8:9], v[8:9], 0, v[156:157]
	v_addc_co_u32_e64 v11, s[0:1], 0, v11, s[0:1]
	v_or3_b32 v163, v12, v1, v0
	global_load_dwordx4 v[12:15], v[2:3], off
	global_load_dwordx4 v[16:19], v[2:3], off offset:1024
	global_load_dwordx4 v[20:23], v[2:3], off offset:2048
	global_load_dwordx4 v[24:27], v[2:3], off offset:3072
	global_load_dwordx4 v[28:31], v[6:7], off offset:-4096
	global_load_dwordx4 v[32:35], v[6:7], off
	global_load_dwordx4 v[36:39], v[6:7], off offset:1024
	global_load_dwordx4 v[40:43], v[6:7], off offset:2048
	global_load_dwordx4 v[44:47], v[6:7], off offset:3072
	global_load_dwordx4 v[48:51], v[4:5], off offset:1024
	global_load_dwordx4 v[52:55], v[4:5], off offset:2048
	global_load_dwordx4 v[56:59], v[4:5], off offset:3072
	global_load_dwordx4 v[60:63], v[8:9], off
	global_load_dwordx4 v[64:67], v[8:9], off offset:1024
	global_load_dwordx4 v[68:71], v[8:9], off offset:2048
	global_load_dwordx4 v[76:79], v[72:73], off offset:512
	global_load_dwordx4 v[80:83], v[72:73], off offset:1024
	global_load_dwordx4 v[84:87], v[10:11], off
	global_load_dwordx4 v[88:91], v[72:73], off offset:1536
	s_and_b64 s[0:1], vcc, exec
	s_cselect_b32 s14, 0, 0x7f
	s_lshl_b32 s7, s16, 22
	s_add_u32 s0, s8, s7
	s_addc_u32 s1, s9, 0
	v_lshlrev_b32_e32 v94, 12, v108
	v_mov_b32_e32 v95, v157
	v_lshl_add_u64 v[0:1], s[0:1], 0, v[94:95]
	v_lshl_add_u64 v[0:1], v[0:1], 0, v[156:157]
	s_mov_b64 s[0:1], 0xc9000
	v_lshl_add_u64 v[158:159], v[0:1], 0, s[0:1]
	s_lshl_b32 s4, s14, 15
	v_lshl_add_u64 v[96:97], v[158:159], 0, s[4:5]
	global_load_dwordx4 v[72:75], v[96:97], off
	global_load_dwordx4 v[8:11], v[96:97], off offset:1024
	global_load_dwordx4 v[4:7], v[96:97], off offset:2048
	global_load_dwordx4 v[0:3], v[96:97], off offset:3072
	v_mul_u32_u24_e32 v95, 0x104, v161
	ds_read_b32 v96, v95 offset:16512
	ds_read_b32 v95, v95 offset:20672
	s_movk_i32 s6, 0x410
	s_movk_i32 s0, 0x104
	v_mov_b32_e32 v97, 0x4080
	s_waitcnt lgkmcnt(1)
	v_lshrrev_b32_e32 v178, 16, v96
	v_and_b32_e32 v96, 0xffff, v96
	v_mad_u32_u24 v176, v161, s0, v97
	v_mad_u32_u24 v110, v109, s6, v96
	s_waitcnt lgkmcnt(0)
	v_lshrrev_b32_e32 v177, 16, v95
	v_and_b32_e32 v95, 0xffff, v95
	s_and_b64 s[0:1], vcc, exec
	v_mad_u32_u24 v111, v109, s6, v95
	s_cselect_b32 s15, 1, -1
	s_or_b32 s0, s7, s4
	ds_read_b128 v[120:123], v110 offset:8192
	ds_read_b128 v[116:119], v111 offset:8192
	v_lshl_add_u64 v[164:165], v[92:93], 0, v[156:157]
	v_or3_b32 v92, s0, v94, v156
	v_mov_b32_e32 v93, v157
	v_lshl_add_u64 v[92:93], s[8:9], 0, v[92:93]
	s_mov_b64 s[0:1], 0xc9800
	s_lshl_b32 s4, s15, 1
	v_mov_b32_e32 v106, v157
	v_mov_b32_e32 v107, v157
	v_lshl_add_u64 v[166:167], v[92:93], 0, s[0:1]
	s_ashr_i32 s5, s4, 31
	v_mov_b32_e32 v100, 0xc47a0000
	v_mov_b32_e32 v104, v157
	v_mov_b32_e32 v105, v157
	v_cndmask_b32_e64 v92, 0, 1, s[12:13]
	v_mov_b64_e32 v[142:143], v[106:107]
	s_lshl_b64 s[6:7], s[4:5], 15
	s_add_i32 s8, s14, s15
	v_mov_b32_e32 v101, v100
	v_mov_b32_e32 v102, v100
	v_mov_b32_e32 v103, v100
	s_mov_b32 s5, -2
	v_cmp_ne_u32_e64 s[0:1], 1, v92
	v_mov_b32_e32 v172, v157
	v_mov_b32_e32 v173, v157
	v_mov_b32_e32 v174, v157
	v_mov_b32_e32 v175, v157
	v_mov_b32_e32 v96, v157
	v_mov_b32_e32 v97, v157
	v_mov_b32_e32 v98, v157
	v_mov_b32_e32 v99, v157
	v_mov_b32_e32 v92, v157
	v_mov_b32_e32 v93, v157
	v_mov_b32_e32 v94, v157
	v_mov_b32_e32 v95, v157
	v_mov_b32_e32 v144, v157
	v_mov_b32_e32 v145, v157
	v_mov_b32_e32 v146, v157
	v_mov_b32_e32 v147, v157
	v_mov_b32_e32 v132, v157
	v_mov_b32_e32 v133, v157
	v_mov_b32_e32 v134, v157
	v_mov_b32_e32 v135, v157
	v_mov_b32_e32 v128, v157
	v_mov_b32_e32 v129, v157
	v_mov_b32_e32 v130, v157
	v_mov_b32_e32 v131, v157
	v_mov_b32_e32 v136, v157
	v_mov_b32_e32 v137, v157
	v_mov_b32_e32 v138, v157
	v_mov_b32_e32 v139, v157
	v_mov_b32_e32 v124, v157
	v_mov_b32_e32 v125, v157
	v_mov_b32_e32 v126, v157
	v_mov_b32_e32 v127, v157
	v_mov_b32_e32 v170, v157
	v_mov_b32_e32 v171, v157
	v_mov_b32_e32 v168, v157
	v_mov_b32_e32 v169, v157
	v_lshlrev_b32_e32 v162, 4, v108
	v_mul_u32_u24_e32 v157, 0x410, v109
	v_lshlrev_b32_e32 v160, 2, v109
	v_mov_b64_e32 v[140:141], v[104:105]
	v_mov_b32_e32 v144, 0
	v_mov_b32_e32 v145, 0
	v_mov_b32_e32 v146, 0
	v_mov_b32_e32 v147, 0
	v_mov_b32_e32 v148, 0xc47a0000
	v_mov_b32_e32 v149, 0xc47a0000
	v_mov_b32_e32 v150, 0xc47a0000
	v_mov_b32_e32 v151, 0xc47a0000
	v_mov_b32_e32 v152, 0
	v_mov_b32_e32 v153, 0
	v_mov_b32_e32 v154, 0
	v_mov_b32_e32 v155, 0
	s_movk_i32 s17, 0x61
	global_load_dwordx4 v[206:209], v[164:165], off
	global_load_dwordx4 v[210:213], v[164:165], off offset:1024
	global_load_dwordx4 v[214:217], v[164:165], off offset:2048
	v_add_u32_e32 v226, v162, v160
	v_mul_u32_u24_e32 v226, 12, v226
	v_lshl_add_u32 v229, v161, 4, v157
	v_mul_u32_u24_e32 v230, 0x610, v161
	v_add_u32_e32 v230, v230, v226
	v_add_u32_e32 v231, 0x18400, v226
	s_waitcnt vmcnt(0) lgkmcnt(0)
	ds_read_b128 v[190:193], v229 offset:8192
	s_waitcnt lgkmcnt(0)
	v_mfma_f32_16x16x32_f16 v[194:197], v[60:63], v[190:193], v[84:87]
	v_mfma_f32_16x16x32_f16 v[198:201], v[64:67], v[190:193], v[76:79]
	v_mfma_f32_16x16x32_f16 v[202:205], v[68:71], v[190:193], v[88:91]
	s_nop 7
	s_nop 1
	ds_write_b128 v230, v[194:197] offset:24848
	ds_write_b128 v230, v[198:201] offset:24864
	ds_write_b128 v230, v[202:205] offset:24880
	v_add_u32_e32 v230, 0x6100, v230
	ds_read_b128 v[190:193], v229 offset:8448
	s_waitcnt lgkmcnt(0)
	v_mfma_f32_16x16x32_f16 v[194:197], v[60:63], v[190:193], v[84:87]
	v_mfma_f32_16x16x32_f16 v[198:201], v[64:67], v[190:193], v[76:79]
	v_mfma_f32_16x16x32_f16 v[202:205], v[68:71], v[190:193], v[88:91]
	s_nop 7
	s_nop 1
	ds_write_b128 v230, v[194:197] offset:24848
	ds_write_b128 v230, v[198:201] offset:24864
	ds_write_b128 v230, v[202:205] offset:24880
	v_add_u32_e32 v230, 0x6100, v230
	ds_read_b128 v[190:193], v229 offset:12864
	s_waitcnt lgkmcnt(0)
	v_mfma_f32_16x16x32_f16 v[194:197], v[206:209], v[190:193], v[84:87]
	v_mfma_f32_16x16x32_f16 v[198:201], v[210:213], v[190:193], v[76:79]
	v_mfma_f32_16x16x32_f16 v[202:205], v[214:217], v[190:193], v[88:91]
	s_nop 7
	s_nop 1
	ds_write_b128 v230, v[194:197] offset:24848
	ds_write_b128 v230, v[198:201] offset:24864
	ds_write_b128 v230, v[202:205] offset:24880
	v_add_u32_e32 v230, 0x6100, v230
	ds_read_b128 v[190:193], v229 offset:13120
	s_waitcnt lgkmcnt(0)
	v_mfma_f32_16x16x32_f16 v[194:197], v[206:209], v[190:193], v[84:87]
	v_mfma_f32_16x16x32_f16 v[198:201], v[210:213], v[190:193], v[76:79]
	v_mfma_f32_16x16x32_f16 v[202:205], v[214:217], v[190:193], v[88:91]
	s_nop 7
	s_nop 1
	ds_write_b128 v230, v[194:197] offset:24848
	ds_write_b128 v230, v[198:201] offset:24864
	ds_write_b128 v230, v[202:205] offset:24880
	ds_write_b128 v231, v[84:87] offset:24848
	ds_write_b128 v231, v[76:79] offset:24864
	ds_write_b128 v231, v[88:91] offset:24880
	ds_read_u16 v232, v176
	ds_read_u16 v177, v176 offset:4160
	s_waitcnt lgkmcnt(0)
	v_mad_u32_u24 v227, v232, s17, v226
	ds_read_b128 v[116:119], v227 offset:24848
	ds_read_b128 v[120:123], v227 offset:24864
	ds_read_b128 v[138:141], v227 offset:24880
	v_mov_b32_e32 v182, 0
	v_mov_b32_e32 v183, 0
	v_mov_b32_e32 v184, 0
	v_mov_b32_e32 v185, 0
	v_mov_b32_e32 v222, 0
	v_mov_b32_e32 v223, 0
	v_mov_b32_e32 v224, 0
	v_mov_b32_e32 v225, 0
	v_mov_b32_e32 v186, 0
	v_mov_b32_e32 v187, 0
	v_mov_b32_e32 v188, 0
	v_mov_b32_e32 v189, 0
	v_mov_b32_e32 v100, 0
	v_mov_b32_e32 v101, 0
	v_mov_b32_e32 v102, 0
	v_mov_b32_e32 v103, 0
	v_mov_b32_e32 v104, 0
	v_mov_b32_e32 v105, 0
	v_mov_b32_e32 v106, 0
	v_mov_b32_e32 v107, 0
	v_mov_b32_e32 v108, 0
	v_mov_b32_e32 v109, 0
	v_mov_b32_e32 v110, 0
	v_mov_b32_e32 v111, 0
	v_mov_b32_e32 v112, 0
	v_mov_b32_e32 v113, 0
	v_mov_b32_e32 v114, 0
	v_mov_b32_e32 v115, 0
	v_mov_b32_e32 v206, 0
	v_mov_b32_e32 v207, 0
	v_mov_b32_e32 v208, 0
	v_mov_b32_e32 v209, 0
	v_mov_b32_e32 v210, 0
	v_mov_b32_e32 v211, 0
	v_mov_b32_e32 v212, 0
	v_mov_b32_e32 v213, 0
	v_mov_b32_e32 v214, 0
	v_mov_b32_e32 v215, 0
	v_mov_b32_e32 v216, 0
	v_mov_b32_e32 v217, 0
	v_mov_b32_e32 v218, 0
	v_mov_b32_e32 v219, 0
	v_mov_b32_e32 v220, 0
	v_mov_b32_e32 v221, 0
	s_waitcnt vmcnt(4) lgkmcnt(0)
	v_readfirstlane_b32 s18, v162
	s_nop 3
	s_cmp_ge_u32 s18, 64
	s_cbranch_scc1 .Lgru_loop_b
.Lgru_loop_a:
	s_waitcnt vmcnt(4)
	v_mfma_f32_16x16x32_f16 v[92:95], v[112:115], v[206:209], v[92:95]
	v_exp_f32_e32 v228, v144
	v_exp_f32_e32 v229, v145
	v_exp_f32_e32 v230, v146
	v_exp_f32_e32 v231, v147
	v_exp_f32_e32 v232, v148
	v_exp_f32_e32 v233, v149
	v_exp_f32_e32 v234, v150
	v_exp_f32_e32 v235, v151
	v_mfma_f32_16x16x32_f16 v[92:95], v[108:111], v[210:213], v[92:95]
	v_add_f32_e32 v228, 1.0, v228
	v_add_f32_e32 v229, 1.0, v229
	v_add_f32_e32 v230, 1.0, v230
	v_add_f32_e32 v231, 1.0, v231
	v_add_f32_e32 v232, 1.0, v232
	v_add_f32_e32 v233, 1.0, v233
	v_add_f32_e32 v234, 1.0, v234
	v_add_f32_e32 v235, 1.0, v235
	v_rcp_f32_e32 v228, v228
	v_rcp_f32_e32 v229, v229
	v_rcp_f32_e32 v230, v230
	v_rcp_f32_e32 v231, v231
	v_mfma_f32_16x16x32_f16 v[92:95], v[104:107], v[214:217], v[92:95]
	v_fma_f32 v236, v228, v152, v182
	v_fma_f32 v237, v229, v153, v183
	v_fma_f32 v238, v230, v154, v184
	v_fma_f32 v239, v231, v155, v185
	v_mad_u32_u24 v227, v177, s17, v226
	ds_read_b128 v[222:225], v227 offset:24848
	ds_read_b128 v[186:189], v227 offset:24864
	ds_read_b128 v[182:185], v227 offset:24880
	ds_read_u16 v177, v176 offset:4162
	v_exp_f32_e32 v236, v236
	v_exp_f32_e32 v237, v237
	v_exp_f32_e32 v238, v238
	v_exp_f32_e32 v239, v239
	v_rcp_f32_e32 v232, v232
	v_rcp_f32_e32 v233, v233
	v_mfma_f32_16x16x32_f16 v[92:95], v[100:103], v[218:221], v[92:95]
	global_load_dwordx4 v[112:115], v[166:167], off offset:-2048
	global_load_dwordx4 v[108:111], v[166:167], off offset:-1024
	global_load_dwordx4 v[104:107], v[166:167], off
	global_load_dwordx4 v[100:103], v[166:167], off offset:1024
	v_rcp_f32_e32 v234, v234
	v_rcp_f32_e32 v235, v235
	v_add_f32_e32 v236, 1.0, v236
	v_add_f32_e32 v237, 1.0, v237
	v_add_f32_e32 v238, 1.0, v238
	v_add_f32_e32 v239, 1.0, v239
	v_rcp_f32_e32 v236, v236
	v_rcp_f32_e32 v237, v237
	v_rcp_f32_e32 v238, v238
	v_rcp_f32_e32 v239, v239
	v_pk_fma_f32 v[236:237], v[236:237], -2.0, 1.0 op_sel_hi:[1,0,0]
	v_pk_fma_f32 v[238:239], v[238:239], -2.0, 1.0 op_sel_hi:[1,0,0]
	v_pk_add_f32 v[240:241], v[168:169], v[236:237] neg_lo:[0,1] neg_hi:[0,1]
	v_pk_add_f32 v[242:243], v[170:171], v[238:239] neg_lo:[0,1] neg_hi:[0,1]
	v_pk_fma_f32 v[168:169], v[232:233], v[240:241], v[236:237]
	v_pk_fma_f32 v[170:171], v[234:235], v[242:243], v[238:239]
	v_cvt_pk_f16_f32 v244, v168, v169
	v_cvt_pk_f16_f32 v245, v170, v171
	ds_read_b128 v[190:193], v156 offset:0
	ds_read_b128 v[194:197], v156 offset:1024
	ds_read_b128 v[198:201], v156 offset:2048
	ds_read_b128 v[202:205], v156 offset:3072
	ds_write_b64 v163, v[244:245] offset:4096
	s_waitcnt lgkmcnt(4)
	v_mfma_f32_16x16x32_f16 v[124:127], v[12:15], v[190:193], v[116:119]
	v_mfma_f32_16x16x32_f16 v[128:131], v[28:31], v[190:193], v[120:123]
	v_mfma_f32_16x16x32_f16 v[132:135], v[32:35], v[190:193], v[80:83]
	s_waitcnt lgkmcnt(3)
	v_mfma_f32_16x16x32_f16 v[124:127], v[16:19], v[194:197], v[124:127]
	v_mfma_f32_16x16x32_f16 v[128:131], v[48:51], v[194:197], v[128:131]
	v_mfma_f32_16x16x32_f16 v[132:135], v[36:39], v[194:197], v[132:135]
	s_waitcnt lgkmcnt(2)
	v_mfma_f32_16x16x32_f16 v[124:127], v[20:23], v[198:201], v[124:127]
	v_mfma_f32_16x16x32_f16 v[128:131], v[52:55], v[198:201], v[128:131]
	v_mfma_f32_16x16x32_f16 v[132:135], v[40:43], v[198:201], v[132:135]
	s_waitcnt lgkmcnt(1)
	v_mfma_f32_16x16x32_f16 v[124:127], v[24:27], v[202:205], v[124:127]
	v_mfma_f32_16x16x32_f16 v[128:131], v[56:59], v[202:205], v[128:131]
	v_mfma_f32_16x16x32_f16 v[132:135], v[44:47], v[202:205], v[132:135]
	s_waitcnt lgkmcnt(0)
	s_barrier
	s_waitcnt vmcnt(4)
	v_mfma_f32_16x16x32_f16 v[96:99], v[72:75], v[190:193], v[96:99]
	v_exp_f32_e32 v228, v124
	v_exp_f32_e32 v229, v125
	v_exp_f32_e32 v230, v126
	v_exp_f32_e32 v231, v127
	v_exp_f32_e32 v232, v128
	v_exp_f32_e32 v233, v129
	v_exp_f32_e32 v234, v130
	v_exp_f32_e32 v235, v131
	v_mfma_f32_16x16x32_f16 v[96:99], v[8:11], v[194:197], v[96:99]
	v_add_f32_e32 v228, 1.0, v228
	v_add_f32_e32 v229, 1.0, v229
	v_add_f32_e32 v230, 1.0, v230
	v_add_f32_e32 v231, 1.0, v231
	v_add_f32_e32 v232, 1.0, v232
	v_add_f32_e32 v233, 1.0, v233
	v_add_f32_e32 v234, 1.0, v234
	v_add_f32_e32 v235, 1.0, v235
	v_rcp_f32_e32 v228, v228
	v_rcp_f32_e32 v229, v229
	v_rcp_f32_e32 v230, v230
	v_rcp_f32_e32 v231, v231
	v_mfma_f32_16x16x32_f16 v[96:99], v[4:7], v[198:201], v[96:99]
	v_fma_f32 v236, v228, v132, v138
	v_fma_f32 v237, v229, v133, v139
	v_fma_f32 v238, v230, v134, v140
	v_fma_f32 v239, v231, v135, v141
	v_mad_u32_u24 v227, v178, s17, v226
	ds_read_b128 v[116:119], v227 offset:24848
	ds_read_b128 v[120:123], v227 offset:24864
	ds_read_b128 v[138:141], v227 offset:24880
	ds_read_u16 v178, v176 offset:4
	v_exp_f32_e32 v236, v236
	v_exp_f32_e32 v237, v237
	v_exp_f32_e32 v238, v238
	v_exp_f32_e32 v239, v239
	v_rcp_f32_e32 v232, v232
	v_rcp_f32_e32 v233, v233
	v_mfma_f32_16x16x32_f16 v[96:99], v[0:3], v[202:205], v[96:99]
	v_rcp_f32_e32 v234, v234
	v_rcp_f32_e32 v235, v235
	v_add_f32_e32 v236, 1.0, v236
	v_add_f32_e32 v237, 1.0, v237
	v_add_f32_e32 v238, 1.0, v238
	v_add_f32_e32 v239, 1.0, v239
	v_rcp_f32_e32 v236, v236
	v_rcp_f32_e32 v237, v237
	v_rcp_f32_e32 v238, v238
	v_rcp_f32_e32 v239, v239
	v_pk_fma_f32 v[236:237], v[236:237], -2.0, 1.0 op_sel_hi:[1,0,0]
	v_pk_fma_f32 v[238:239], v[238:239], -2.0, 1.0 op_sel_hi:[1,0,0]
	v_pk_add_f32 v[240:241], v[172:173], v[236:237] neg_lo:[0,1] neg_hi:[0,1]
	v_pk_add_f32 v[242:243], v[174:175], v[238:239] neg_lo:[0,1] neg_hi:[0,1]
	v_pk_fma_f32 v[172:173], v[232:233], v[240:241], v[236:237]
	v_pk_fma_f32 v[174:175], v[234:235], v[242:243], v[238:239]
	v_cvt_pk_f16_f32 v244, v172, v173
	v_cvt_pk_f16_f32 v245, v174, v175
	ds_read_b128 v[206:209], v156 offset:4096
	ds_read_b128 v[210:213], v156 offset:5120
	ds_read_b128 v[214:217], v156 offset:6144
	ds_read_b128 v[218:221], v156 offset:7168
	ds_write_b64 v163, v[244:245]
	s_waitcnt lgkmcnt(4)
	v_mfma_f32_16x16x32_f16 v[144:147], v[12:15], v[206:209], v[222:225]
	v_mfma_f32_16x16x32_f16 v[148:151], v[28:31], v[206:209], v[186:189]
	v_mfma_f32_16x16x32_f16 v[152:155], v[32:35], v[206:209], v[80:83]
	s_waitcnt lgkmcnt(3)
	v_mfma_f32_16x16x32_f16 v[144:147], v[16:19], v[210:213], v[144:147]
	v_mfma_f32_16x16x32_f16 v[148:151], v[48:51], v[210:213], v[148:151]
	v_mfma_f32_16x16x32_f16 v[152:155], v[36:39], v[210:213], v[152:155]
	s_waitcnt lgkmcnt(2)
	v_mfma_f32_16x16x32_f16 v[144:147], v[20:23], v[214:217], v[144:147]
	v_mfma_f32_16x16x32_f16 v[148:151], v[52:55], v[214:217], v[148:151]
	v_mfma_f32_16x16x32_f16 v[152:155], v[40:43], v[214:217], v[152:155]
	s_waitcnt lgkmcnt(1)
	v_mfma_f32_16x16x32_f16 v[144:147], v[24:27], v[218:221], v[144:147]
	v_mfma_f32_16x16x32_f16 v[148:151], v[56:59], v[218:221], v[148:151]
	v_mfma_f32_16x16x32_f16 v[152:155], v[44:47], v[218:221], v[152:155]
	s_waitcnt lgkmcnt(0)
	s_barrier
	v_mfma_f32_16x16x32_f16 v[92:95], v[72:75], v[206:209], v[92:95]
	v_exp_f32_e32 v228, v144
	v_exp_f32_e32 v229, v145
	v_exp_f32_e32 v230, v146
	v_exp_f32_e32 v231, v147
	v_exp_f32_e32 v232, v148
	v_exp_f32_e32 v233, v149
	v_exp_f32_e32 v234, v150
	v_exp_f32_e32 v235, v151
	v_mfma_f32_16x16x32_f16 v[92:95], v[8:11], v[210:213], v[92:95]
	v_add_f32_e32 v228, 1.0, v228
	v_add_f32_e32 v229, 1.0, v229
	v_add_f32_e32 v230, 1.0, v230
	v_add_f32_e32 v231, 1.0, v231
	v_add_f32_e32 v232, 1.0, v232
	v_add_f32_e32 v233, 1.0, v233
	v_add_f32_e32 v234, 1.0, v234
	v_add_f32_e32 v235, 1.0, v235
	v_rcp_f32_e32 v228, v228
	v_rcp_f32_e32 v229, v229
	v_rcp_f32_e32 v230, v230
	v_rcp_f32_e32 v231, v231
	v_mfma_f32_16x16x32_f16 v[92:95], v[4:7], v[214:217], v[92:95]
	v_fma_f32 v236, v228, v152, v182
	v_fma_f32 v237, v229, v153, v183
	v_fma_f32 v238, v230, v154, v184
	v_fma_f32 v239, v231, v155, v185
	v_mad_u32_u24 v227, v177, s17, v226
	ds_read_b128 v[222:225], v227 offset:24848
	ds_read_b128 v[186:189], v227 offset:24864
	ds_read_b128 v[182:185], v227 offset:24880
	ds_read_u16 v177, v176 offset:4164
	v_exp_f32_e32 v236, v236
	v_exp_f32_e32 v237, v237
	v_exp_f32_e32 v238, v238
	v_exp_f32_e32 v239, v239
	v_rcp_f32_e32 v232, v232
	v_rcp_f32_e32 v233, v233
	v_mfma_f32_16x16x32_f16 v[92:95], v[0:3], v[218:221], v[92:95]
	s_ashr_i32 s9, s8, 31
	s_lshl_b64 s[12:13], s[8:9], 15
	v_lshl_add_u64 v[246:247], v[158:159], 0, s[12:13]
	global_load_dwordx4 v[72:75], v[246:247], off
	global_load_dwordx4 v[8:11], v[246:247], off offset:1024
	global_load_dwordx4 v[4:7], v[246:247], off offset:2048
	global_load_dwordx4 v[0:3], v[246:247], off offset:3072
	v_rcp_f32_e32 v234, v234
	v_rcp_f32_e32 v235, v235
	v_add_f32_e32 v236, 1.0, v236
	v_add_f32_e32 v237, 1.0, v237
	v_add_f32_e32 v238, 1.0, v238
	v_add_f32_e32 v239, 1.0, v239
	v_rcp_f32_e32 v236, v236
	v_rcp_f32_e32 v237, v237
	v_rcp_f32_e32 v238, v238
	v_rcp_f32_e32 v239, v239
	v_pk_fma_f32 v[236:237], v[236:237], -2.0, 1.0 op_sel_hi:[1,0,0]
	v_pk_fma_f32 v[238:239], v[238:239], -2.0, 1.0 op_sel_hi:[1,0,0]
	v_pk_add_f32 v[240:241], v[168:169], v[236:237] neg_lo:[0,1] neg_hi:[0,1]
	v_pk_add_f32 v[242:243], v[170:171], v[238:239] neg_lo:[0,1] neg_hi:[0,1]
	v_pk_fma_f32 v[168:169], v[232:233], v[240:241], v[236:237]
	v_pk_fma_f32 v[170:171], v[234:235], v[242:243], v[238:239]
	v_cvt_pk_f16_f32 v244, v168, v169
	v_cvt_pk_f16_f32 v245, v170, v171
	ds_read_b128 v[190:193], v156 offset:0
	ds_read_b128 v[194:197], v156 offset:1024
	ds_read_b128 v[198:201], v156 offset:2048
	ds_read_b128 v[202:205], v156 offset:3072
	ds_write_b64 v163, v[244:245] offset:4096
	s_waitcnt lgkmcnt(4)
	v_mfma_f32_16x16x32_f16 v[124:127], v[12:15], v[190:193], v[116:119]
	v_mfma_f32_16x16x32_f16 v[128:131], v[28:31], v[190:193], v[120:123]
	v_mfma_f32_16x16x32_f16 v[132:135], v[32:35], v[190:193], v[80:83]
	s_waitcnt lgkmcnt(3)
	v_mfma_f32_16x16x32_f16 v[124:127], v[16:19], v[194:197], v[124:127]
	v_mfma_f32_16x16x32_f16 v[128:131], v[48:51], v[194:197], v[128:131]
	v_mfma_f32_16x16x32_f16 v[132:135], v[36:39], v[194:197], v[132:135]
	s_waitcnt lgkmcnt(2)
	v_mfma_f32_16x16x32_f16 v[124:127], v[20:23], v[198:201], v[124:127]
	v_mfma_f32_16x16x32_f16 v[128:131], v[52:55], v[198:201], v[128:131]
	v_mfma_f32_16x16x32_f16 v[132:135], v[40:43], v[198:201], v[132:135]
	s_waitcnt lgkmcnt(1)
	v_mfma_f32_16x16x32_f16 v[124:127], v[24:27], v[202:205], v[124:127]
	v_mfma_f32_16x16x32_f16 v[128:131], v[56:59], v[202:205], v[128:131]
	v_mfma_f32_16x16x32_f16 v[132:135], v[44:47], v[202:205], v[132:135]
	s_waitcnt lgkmcnt(0)
	s_barrier
	s_waitcnt vmcnt(4)
	v_mfma_f32_16x16x32_f16 v[96:99], v[112:115], v[190:193], v[96:99]
	v_exp_f32_e32 v228, v124
	v_exp_f32_e32 v229, v125
	v_exp_f32_e32 v230, v126
	v_exp_f32_e32 v231, v127
	v_exp_f32_e32 v232, v128
	v_exp_f32_e32 v233, v129
	v_exp_f32_e32 v234, v130
	v_exp_f32_e32 v235, v131
	v_mfma_f32_16x16x32_f16 v[96:99], v[108:111], v[194:197], v[96:99]
	v_add_f32_e32 v228, 1.0, v228
	v_add_f32_e32 v229, 1.0, v229
	v_add_f32_e32 v230, 1.0, v230
	v_add_f32_e32 v231, 1.0, v231
	v_add_f32_e32 v232, 1.0, v232
	v_add_f32_e32 v233, 1.0, v233
	v_add_f32_e32 v234, 1.0, v234
	v_add_f32_e32 v235, 1.0, v235
	v_rcp_f32_e32 v228, v228
	v_rcp_f32_e32 v229, v229
	v_rcp_f32_e32 v230, v230
	v_rcp_f32_e32 v231, v231
	v_mfma_f32_16x16x32_f16 v[96:99], v[104:107], v[198:201], v[96:99]
	v_fma_f32 v236, v228, v132, v138
	v_fma_f32 v237, v229, v133, v139
	v_fma_f32 v238, v230, v134, v140
	v_fma_f32 v239, v231, v135, v141
	v_mad_u32_u24 v227, v178, s17, v226
	ds_read_b128 v[116:119], v227 offset:24848
	ds_read_b128 v[120:123], v227 offset:24864
	ds_read_b128 v[138:141], v227 offset:24880
	ds_read_u16 v178, v176 offset:6
	v_exp_f32_e32 v236, v236
	v_exp_f32_e32 v237, v237
	v_exp_f32_e32 v238, v238
	v_exp_f32_e32 v239, v239
	v_rcp_f32_e32 v232, v232
	v_rcp_f32_e32 v233, v233
	v_mfma_f32_16x16x32_f16 v[96:99], v[100:103], v[202:205], v[96:99]
	v_rcp_f32_e32 v234, v234
	v_rcp_f32_e32 v235, v235
	v_add_f32_e32 v236, 1.0, v236
	v_add_f32_e32 v237, 1.0, v237
	v_add_f32_e32 v238, 1.0, v238
	v_add_f32_e32 v239, 1.0, v239
	v_rcp_f32_e32 v236, v236
	v_rcp_f32_e32 v237, v237
	v_rcp_f32_e32 v238, v238
	v_rcp_f32_e32 v239, v239
	v_pk_fma_f32 v[236:237], v[236:237], -2.0, 1.0 op_sel_hi:[1,0,0]
	v_pk_fma_f32 v[238:239], v[238:239], -2.0, 1.0 op_sel_hi:[1,0,0]
	v_pk_add_f32 v[240:241], v[172:173], v[236:237] neg_lo:[0,1] neg_hi:[0,1]
	v_pk_add_f32 v[242:243], v[174:175], v[238:239] neg_lo:[0,1] neg_hi:[0,1]
	v_pk_fma_f32 v[172:173], v[232:233], v[240:241], v[236:237]
	v_pk_fma_f32 v[174:175], v[234:235], v[242:243], v[238:239]
	v_cvt_pk_f16_f32 v244, v172, v173
	v_cvt_pk_f16_f32 v245, v174, v175
	ds_read_b128 v[206:209], v156 offset:4096
	ds_read_b128 v[210:213], v156 offset:5120
	ds_read_b128 v[214:217], v156 offset:6144
	ds_read_b128 v[218:221], v156 offset:7168
	ds_write_b64 v163, v[244:245]
	s_waitcnt lgkmcnt(4)
	v_mfma_f32_16x16x32_f16 v[144:147], v[12:15], v[206:209], v[222:225]
	v_mfma_f32_16x16x32_f16 v[148:151], v[28:31], v[206:209], v[186:189]
	v_mfma_f32_16x16x32_f16 v[152:155], v[32:35], v[206:209], v[80:83]
	s_waitcnt lgkmcnt(3)
	v_mfma_f32_16x16x32_f16 v[144:147], v[16:19], v[210:213], v[144:147]
	v_mfma_f32_16x16x32_f16 v[148:151], v[48:51], v[210:213], v[148:151]
	v_mfma_f32_16x16x32_f16 v[152:155], v[36:39], v[210:213], v[152:155]
	s_waitcnt lgkmcnt(2)
	v_mfma_f32_16x16x32_f16 v[144:147], v[20:23], v[214:217], v[144:147]
	v_mfma_f32_16x16x32_f16 v[148:151], v[52:55], v[214:217], v[148:151]
	v_mfma_f32_16x16x32_f16 v[152:155], v[40:43], v[214:217], v[152:155]
	s_waitcnt lgkmcnt(1)
	v_mfma_f32_16x16x32_f16 v[144:147], v[24:27], v[218:221], v[144:147]
	v_mfma_f32_16x16x32_f16 v[148:151], v[56:59], v[218:221], v[148:151]
	v_mfma_f32_16x16x32_f16 v[152:155], v[44:47], v[218:221], v[152:155]
	s_add_i32 s5, s5, 2
	s_add_i32 s8, s8, s4
	v_add_u32_e32 v176, 4, v176
	v_lshl_add_u64 v[166:167], v[166:167], 0, s[6:7]
	s_cmpk_gt_u32 s5, 0x7d
	s_waitcnt lgkmcnt(0)
	s_barrier
	s_cbranch_scc0 .Lgru_loop_a
	s_branch .Lgru_tail
.Lgru_loop_b:
.Lgru_loop_b2:
	ds_read_b128 v[190:193], v156 offset:0
	ds_read_b128 v[194:197], v156 offset:1024
	ds_read_b128 v[198:201], v156 offset:2048
	ds_read_b128 v[202:205], v156 offset:3072
	global_load_dwordx4 v[112:115], v[166:167], off offset:-2048
	global_load_dwordx4 v[108:111], v[166:167], off offset:-1024
	global_load_dwordx4 v[104:107], v[166:167], off
	global_load_dwordx4 v[100:103], v[166:167], off offset:1024
	s_waitcnt lgkmcnt(3)
	v_mfma_f32_16x16x32_f16 v[124:127], v[12:15], v[190:193], v[116:119]
	v_mfma_f32_16x16x32_f16 v[128:131], v[28:31], v[190:193], v[120:123]
	v_mfma_f32_16x16x32_f16 v[132:135], v[32:35], v[190:193], v[80:83]
	s_waitcnt lgkmcnt(2)
	v_mfma_f32_16x16x32_f16 v[124:127], v[16:19], v[194:197], v[124:127]
	v_mfma_f32_16x16x32_f16 v[128:131], v[48:51], v[194:197], v[128:131]
	v_mfma_f32_16x16x32_f16 v[132:135], v[36:39], v[194:197], v[132:135]
	s_waitcnt lgkmcnt(1)
	v_mfma_f32_16x16x32_f16 v[124:127], v[20:23], v[198:201], v[124:127]
	v_mfma_f32_16x16x32_f16 v[128:131], v[52:55], v[198:201], v[128:131]
	v_mfma_f32_16x16x32_f16 v[132:135], v[40:43], v[198:201], v[132:135]
	s_waitcnt lgkmcnt(0)
	v_mfma_f32_16x16x32_f16 v[124:127], v[24:27], v[202:205], v[124:127]
	v_mfma_f32_16x16x32_f16 v[128:131], v[56:59], v[202:205], v[128:131]
	v_mfma_f32_16x16x32_f16 v[132:135], v[44:47], v[202:205], v[132:135]
	v_exp_f32_e32 v228, v144
	v_exp_f32_e32 v229, v145
	v_exp_f32_e32 v230, v146
	v_exp_f32_e32 v231, v147
	v_exp_f32_e32 v232, v148
	v_exp_f32_e32 v233, v149
	v_exp_f32_e32 v234, v150
	v_exp_f32_e32 v235, v151
	v_add_f32_e32 v228, 1.0, v228
	v_add_f32_e32 v229, 1.0, v229
	v_add_f32_e32 v230, 1.0, v230
	v_add_f32_e32 v231, 1.0, v231
	v_add_f32_e32 v232, 1.0, v232
	v_add_f32_e32 v233, 1.0, v233
	v_add_f32_e32 v234, 1.0, v234
	v_add_f32_e32 v235, 1.0, v235
	v_rcp_f32_e32 v228, v228
	v_rcp_f32_e32 v229, v229
	v_rcp_f32_e32 v230, v230
	v_rcp_f32_e32 v231, v231
	v_fma_f32 v236, v228, v152, v182
	v_fma_f32 v237, v229, v153, v183
	v_fma_f32 v238, v230, v154, v184
	v_fma_f32 v239, v231, v155, v185
	v_mad_u32_u24 v227, v177, s17, v226
	ds_read_b128 v[222:225], v227 offset:24848
	ds_read_b128 v[186:189], v227 offset:24864
	ds_read_b128 v[182:185], v227 offset:24880
	ds_read_u16 v177, v176 offset:4162
	v_exp_f32_e32 v236, v236
	v_exp_f32_e32 v237, v237
	v_exp_f32_e32 v238, v238
	v_exp_f32_e32 v239, v239
	v_rcp_f32_e32 v232, v232
	v_rcp_f32_e32 v233, v233
	v_rcp_f32_e32 v234, v234
	v_rcp_f32_e32 v235, v235
	v_add_f32_e32 v236, 1.0, v236
	v_add_f32_e32 v237, 1.0, v237
	v_add_f32_e32 v238, 1.0, v238
	v_add_f32_e32 v239, 1.0, v239
	v_rcp_f32_e32 v236, v236
	v_rcp_f32_e32 v237, v237
	v_rcp_f32_e32 v238, v238
	v_rcp_f32_e32 v239, v239
	v_pk_fma_f32 v[236:237], v[236:237], -2.0, 1.0 op_sel_hi:[1,0,0]
	v_pk_fma_f32 v[238:239], v[238:239], -2.0, 1.0 op_sel_hi:[1,0,0]
	v_pk_add_f32 v[240:241], v[168:169], v[236:237] neg_lo:[0,1] neg_hi:[0,1]
	v_pk_add_f32 v[242:243], v[170:171], v[238:239] neg_lo:[0,1] neg_hi:[0,1]
	v_pk_fma_f32 v[168:169], v[232:233], v[240:241], v[236:237]
	v_pk_fma_f32 v[170:171], v[234:235], v[242:243], v[238:239]
	v_cvt_pk_f16_f32 v244, v168, v169
	v_cvt_pk_f16_f32 v245, v170, v171
	ds_write_b64 v163, v[244:245] offset:4096
	s_waitcnt vmcnt(4)
	v_mfma_f32_16x16x32_f16 v[96:99], v[72:75], v[190:193], v[96:99]
	v_mfma_f32_16x16x32_f16 v[96:99], v[8:11], v[194:197], v[96:99]
	v_mfma_f32_16x16x32_f16 v[96:99], v[4:7], v[198:201], v[96:99]
	v_mfma_f32_16x16x32_f16 v[96:99], v[0:3], v[202:205], v[96:99]
	s_waitcnt lgkmcnt(0)
	s_barrier
	ds_read_b128 v[206:209], v156 offset:4096
	ds_read_b128 v[210:213], v156 offset:5120
	ds_read_b128 v[214:217], v156 offset:6144
	ds_read_b128 v[218:221], v156 offset:7168
	s_waitcnt lgkmcnt(3)
	v_mfma_f32_16x16x32_f16 v[144:147], v[12:15], v[206:209], v[222:225]
	v_mfma_f32_16x16x32_f16 v[148:151], v[28:31], v[206:209], v[186:189]
	v_mfma_f32_16x16x32_f16 v[152:155], v[32:35], v[206:209], v[80:83]
	s_waitcnt lgkmcnt(2)
	v_mfma_f32_16x16x32_f16 v[144:147], v[16:19], v[210:213], v[144:147]
	v_mfma_f32_16x16x32_f16 v[148:151], v[48:51], v[210:213], v[148:151]
	v_mfma_f32_16x16x32_f16 v[152:155], v[36:39], v[210:213], v[152:155]
	s_waitcnt lgkmcnt(1)
	v_mfma_f32_16x16x32_f16 v[144:147], v[20:23], v[214:217], v[144:147]
	v_mfma_f32_16x16x32_f16 v[148:151], v[52:55], v[214:217], v[148:151]
	v_mfma_f32_16x16x32_f16 v[152:155], v[40:43], v[214:217], v[152:155]
	s_waitcnt lgkmcnt(0)
	v_mfma_f32_16x16x32_f16 v[144:147], v[24:27], v[218:221], v[144:147]
	v_mfma_f32_16x16x32_f16 v[148:151], v[56:59], v[218:221], v[148:151]
	v_mfma_f32_16x16x32_f16 v[152:155], v[44:47], v[218:221], v[152:155]
	v_exp_f32_e32 v228, v124
	v_exp_f32_e32 v229, v125
	v_exp_f32_e32 v230, v126
	v_exp_f32_e32 v231, v127
	v_exp_f32_e32 v232, v128
	v_exp_f32_e32 v233, v129
	v_exp_f32_e32 v234, v130
	v_exp_f32_e32 v235, v131
	v_add_f32_e32 v228, 1.0, v228
	v_add_f32_e32 v229, 1.0, v229
	v_add_f32_e32 v230, 1.0, v230
	v_add_f32_e32 v231, 1.0, v231
	v_add_f32_e32 v232, 1.0, v232
	v_add_f32_e32 v233, 1.0, v233
	v_add_f32_e32 v234, 1.0, v234
	v_add_f32_e32 v235, 1.0, v235
	v_rcp_f32_e32 v228, v228
	v_rcp_f32_e32 v229, v229
	v_rcp_f32_e32 v230, v230
	v_rcp_f32_e32 v231, v231
	v_fma_f32 v236, v228, v132, v138
	v_fma_f32 v237, v229, v133, v139
	v_fma_f32 v238, v230, v134, v140
	v_fma_f32 v239, v231, v135, v141
	v_mad_u32_u24 v227, v178, s17, v226
	ds_read_b128 v[116:119], v227 offset:24848
	ds_read_b128 v[120:123], v227 offset:24864
	ds_read_b128 v[138:141], v227 offset:24880
	ds_read_u16 v178, v176 offset:4
	v_exp_f32_e32 v236, v236
	v_exp_f32_e32 v237, v237
	v_exp_f32_e32 v238, v238
	v_exp_f32_e32 v239, v239
	v_rcp_f32_e32 v232, v232
	v_rcp_f32_e32 v233, v233
	v_rcp_f32_e32 v234, v234
	v_rcp_f32_e32 v235, v235
	v_add_f32_e32 v236, 1.0, v236
	v_add_f32_e32 v237, 1.0, v237
	v_add_f32_e32 v238, 1.0, v238
	v_add_f32_e32 v239, 1.0, v239
	v_rcp_f32_e32 v236, v236
	v_rcp_f32_e32 v237, v237
	v_rcp_f32_e32 v238, v238
	v_rcp_f32_e32 v239, v239
	v_pk_fma_f32 v[236:237], v[236:237], -2.0, 1.0 op_sel_hi:[1,0,0]
	v_pk_fma_f32 v[238:239], v[238:239], -2.0, 1.0 op_sel_hi:[1,0,0]
	v_pk_add_f32 v[240:241], v[172:173], v[236:237] neg_lo:[0,1] neg_hi:[0,1]
	v_pk_add_f32 v[242:243], v[174:175], v[238:239] neg_lo:[0,1] neg_hi:[0,1]
	v_pk_fma_f32 v[172:173], v[232:233], v[240:241], v[236:237]
	v_pk_fma_f32 v[174:175], v[234:235], v[242:243], v[238:239]
	v_cvt_pk_f16_f32 v244, v172, v173
	v_cvt_pk_f16_f32 v245, v174, v175
	ds_write_b64 v163, v[244:245]
	s_waitcnt vmcnt(4)
	v_mfma_f32_16x16x32_f16 v[92:95], v[72:75], v[206:209], v[92:95]
	v_mfma_f32_16x16x32_f16 v[92:95], v[8:11], v[210:213], v[92:95]
	v_mfma_f32_16x16x32_f16 v[92:95], v[4:7], v[214:217], v[92:95]
	v_mfma_f32_16x16x32_f16 v[92:95], v[0:3], v[218:221], v[92:95]
	s_waitcnt lgkmcnt(0)
	s_barrier
	ds_read_b128 v[190:193], v156 offset:0
	ds_read_b128 v[194:197], v156 offset:1024
	ds_read_b128 v[198:201], v156 offset:2048
	ds_read_b128 v[202:205], v156 offset:3072
	s_ashr_i32 s9, s8, 31
	s_lshl_b64 s[12:13], s[8:9], 15
	v_lshl_add_u64 v[246:247], v[158:159], 0, s[12:13]
	global_load_dwordx4 v[72:75], v[246:247], off
	global_load_dwordx4 v[8:11], v[246:247], off offset:1024
	global_load_dwordx4 v[4:7], v[246:247], off offset:2048
	global_load_dwordx4 v[0:3], v[246:247], off offset:3072
	s_waitcnt lgkmcnt(3)
	v_mfma_f32_16x16x32_f16 v[124:127], v[12:15], v[190:193], v[116:119]
	v_mfma_f32_16x16x32_f16 v[128:131], v[28:31], v[190:193], v[120:123]
	v_mfma_f32_16x16x32_f16 v[132:135], v[32:35], v[190:193], v[80:83]
	s_waitcnt lgkmcnt(2)
	v_mfma_f32_16x16x32_f16 v[124:127], v[16:19], v[194:197], v[124:127]
	v_mfma_f32_16x16x32_f16 v[128:131], v[48:51], v[194:197], v[128:131]
	v_mfma_f32_16x16x32_f16 v[132:135], v[36:39], v[194:197], v[132:135]
	s_waitcnt lgkmcnt(1)
	v_mfma_f32_16x16x32_f16 v[124:127], v[20:23], v[198:201], v[124:127]
	v_mfma_f32_16x16x32_f16 v[128:131], v[52:55], v[198:201], v[128:131]
	v_mfma_f32_16x16x32_f16 v[132:135], v[40:43], v[198:201], v[132:135]
	s_waitcnt lgkmcnt(0)
	v_mfma_f32_16x16x32_f16 v[124:127], v[24:27], v[202:205], v[124:127]
	v_mfma_f32_16x16x32_f16 v[128:131], v[56:59], v[202:205], v[128:131]
	v_mfma_f32_16x16x32_f16 v[132:135], v[44:47], v[202:205], v[132:135]
	v_exp_f32_e32 v228, v144
	v_exp_f32_e32 v229, v145
	v_exp_f32_e32 v230, v146
	v_exp_f32_e32 v231, v147
	v_exp_f32_e32 v232, v148
	v_exp_f32_e32 v233, v149
	v_exp_f32_e32 v234, v150
	v_exp_f32_e32 v235, v151
	v_add_f32_e32 v228, 1.0, v228
	v_add_f32_e32 v229, 1.0, v229
	v_add_f32_e32 v230, 1.0, v230
	v_add_f32_e32 v231, 1.0, v231
	v_add_f32_e32 v232, 1.0, v232
	v_add_f32_e32 v233, 1.0, v233
	v_add_f32_e32 v234, 1.0, v234
	v_add_f32_e32 v235, 1.0, v235
	v_rcp_f32_e32 v228, v228
	v_rcp_f32_e32 v229, v229
	v_rcp_f32_e32 v230, v230
	v_rcp_f32_e32 v231, v231
	v_fma_f32 v236, v228, v152, v182
	v_fma_f32 v237, v229, v153, v183
	v_fma_f32 v238, v230, v154, v184
	v_fma_f32 v239, v231, v155, v185
	v_mad_u32_u24 v227, v177, s17, v226
	ds_read_b128 v[222:225], v227 offset:24848
	ds_read_b128 v[186:189], v227 offset:24864
	ds_read_b128 v[182:185], v227 offset:24880
	ds_read_u16 v177, v176 offset:4164
	v_exp_f32_e32 v236, v236
	v_exp_f32_e32 v237, v237
	v_exp_f32_e32 v238, v238
	v_exp_f32_e32 v239, v239
	v_rcp_f32_e32 v232, v232
	v_rcp_f32_e32 v233, v233
	v_rcp_f32_e32 v234, v234
	v_rcp_f32_e32 v235, v235
	v_add_f32_e32 v236, 1.0, v236
	v_add_f32_e32 v237, 1.0, v237
	v_add_f32_e32 v238, 1.0, v238
	v_add_f32_e32 v239, 1.0, v239
	v_rcp_f32_e32 v236, v236
	v_rcp_f32_e32 v237, v237
	v_rcp_f32_e32 v238, v238
	v_rcp_f32_e32 v239, v239
	v_pk_fma_f32 v[236:237], v[236:237], -2.0, 1.0 op_sel_hi:[1,0,0]
	v_pk_fma_f32 v[238:239], v[238:239], -2.0, 1.0 op_sel_hi:[1,0,0]
	v_pk_add_f32 v[240:241], v[168:169], v[236:237] neg_lo:[0,1] neg_hi:[0,1]
	v_pk_add_f32 v[242:243], v[170:171], v[238:239] neg_lo:[0,1] neg_hi:[0,1]
	v_pk_fma_f32 v[168:169], v[232:233], v[240:241], v[236:237]
	v_pk_fma_f32 v[170:171], v[234:235], v[242:243], v[238:239]
	v_cvt_pk_f16_f32 v244, v168, v169
	v_cvt_pk_f16_f32 v245, v170, v171
	ds_write_b64 v163, v[244:245] offset:4096
	s_waitcnt vmcnt(4)
	v_mfma_f32_16x16x32_f16 v[96:99], v[112:115], v[190:193], v[96:99]
	v_mfma_f32_16x16x32_f16 v[96:99], v[108:111], v[194:197], v[96:99]
	v_mfma_f32_16x16x32_f16 v[96:99], v[104:107], v[198:201], v[96:99]
	v_mfma_f32_16x16x32_f16 v[96:99], v[100:103], v[202:205], v[96:99]
	s_waitcnt lgkmcnt(0)
	s_barrier
	ds_read_b128 v[206:209], v156 offset:4096
	ds_read_b128 v[210:213], v156 offset:5120
	ds_read_b128 v[214:217], v156 offset:6144
	ds_read_b128 v[218:221], v156 offset:7168
	s_waitcnt lgkmcnt(3)
	v_mfma_f32_16x16x32_f16 v[144:147], v[12:15], v[206:209], v[222:225]
	v_mfma_f32_16x16x32_f16 v[148:151], v[28:31], v[206:209], v[186:189]
	v_mfma_f32_16x16x32_f16 v[152:155], v[32:35], v[206:209], v[80:83]
	s_waitcnt lgkmcnt(2)
	v_mfma_f32_16x16x32_f16 v[144:147], v[16:19], v[210:213], v[144:147]
	v_mfma_f32_16x16x32_f16 v[148:151], v[48:51], v[210:213], v[148:151]
	v_mfma_f32_16x16x32_f16 v[152:155], v[36:39], v[210:213], v[152:155]
	s_waitcnt lgkmcnt(1)
	v_mfma_f32_16x16x32_f16 v[144:147], v[20:23], v[214:217], v[144:147]
	v_mfma_f32_16x16x32_f16 v[148:151], v[52:55], v[214:217], v[148:151]
	v_mfma_f32_16x16x32_f16 v[152:155], v[40:43], v[214:217], v[152:155]
	s_waitcnt lgkmcnt(0)
	v_mfma_f32_16x16x32_f16 v[144:147], v[24:27], v[218:221], v[144:147]
	v_mfma_f32_16x16x32_f16 v[148:151], v[56:59], v[218:221], v[148:151]
	v_mfma_f32_16x16x32_f16 v[152:155], v[44:47], v[218:221], v[152:155]
	v_exp_f32_e32 v228, v124
	v_exp_f32_e32 v229, v125
	v_exp_f32_e32 v230, v126
	v_exp_f32_e32 v231, v127
	v_exp_f32_e32 v232, v128
	v_exp_f32_e32 v233, v129
	v_exp_f32_e32 v234, v130
	v_exp_f32_e32 v235, v131
	v_add_f32_e32 v228, 1.0, v228
	v_add_f32_e32 v229, 1.0, v229
	v_add_f32_e32 v230, 1.0, v230
	v_add_f32_e32 v231, 1.0, v231
	v_add_f32_e32 v232, 1.0, v232
	v_add_f32_e32 v233, 1.0, v233
	v_add_f32_e32 v234, 1.0, v234
	v_add_f32_e32 v235, 1.0, v235
	v_rcp_f32_e32 v228, v228
	v_rcp_f32_e32 v229, v229
	v_rcp_f32_e32 v230, v230
	v_rcp_f32_e32 v231, v231
	v_fma_f32 v236, v228, v132, v138
	v_fma_f32 v237, v229, v133, v139
	v_fma_f32 v238, v230, v134, v140
	v_fma_f32 v239, v231, v135, v141
	v_mad_u32_u24 v227, v178, s17, v226
	ds_read_b128 v[116:119], v227 offset:24848
	ds_read_b128 v[120:123], v227 offset:24864
	ds_read_b128 v[138:141], v227 offset:24880
	ds_read_u16 v178, v176 offset:6
	v_exp_f32_e32 v236, v236
	v_exp_f32_e32 v237, v237
	v_exp_f32_e32 v238, v238
	v_exp_f32_e32 v239, v239
	v_rcp_f32_e32 v232, v232
	v_rcp_f32_e32 v233, v233
	v_rcp_f32_e32 v234, v234
	v_rcp_f32_e32 v235, v235
	v_add_f32_e32 v236, 1.0, v236
	v_add_f32_e32 v237, 1.0, v237
	v_add_f32_e32 v238, 1.0, v238
	v_add_f32_e32 v239, 1.0, v239
	v_rcp_f32_e32 v236, v236
	v_rcp_f32_e32 v237, v237
	v_rcp_f32_e32 v238, v238
	v_rcp_f32_e32 v239, v239
	v_pk_fma_f32 v[236:237], v[236:237], -2.0, 1.0 op_sel_hi:[1,0,0]
	v_pk_fma_f32 v[238:239], v[238:239], -2.0, 1.0 op_sel_hi:[1,0,0]
	v_pk_add_f32 v[240:241], v[172:173], v[236:237] neg_lo:[0,1] neg_hi:[0,1]
	v_pk_add_f32 v[242:243], v[174:175], v[238:239] neg_lo:[0,1] neg_hi:[0,1]
	v_pk_fma_f32 v[172:173], v[232:233], v[240:241], v[236:237]
	v_pk_fma_f32 v[174:175], v[234:235], v[242:243], v[238:239]
	v_cvt_pk_f16_f32 v244, v172, v173
	v_cvt_pk_f16_f32 v245, v174, v175
	ds_write_b64 v163, v[244:245]
	s_waitcnt vmcnt(4)
	v_mfma_f32_16x16x32_f16 v[92:95], v[112:115], v[206:209], v[92:95]
	v_mfma_f32_16x16x32_f16 v[92:95], v[108:111], v[210:213], v[92:95]
	v_mfma_f32_16x16x32_f16 v[92:95], v[104:107], v[214:217], v[92:95]
	v_mfma_f32_16x16x32_f16 v[92:95], v[100:103], v[218:221], v[92:95]
	s_add_i32 s5, s5, 2
	s_add_i32 s8, s8, s4
	v_add_u32_e32 v176, 4, v176
	v_lshl_add_u64 v[166:167], v[166:167], 0, s[6:7]
	s_cmpk_gt_u32 s5, 0x7d
	s_waitcnt lgkmcnt(0)
	s_barrier
	s_cbranch_scc0 .Lgru_loop_b2
	s_waitcnt vmcnt(0)
	s_branch .Lgru_tail2

.Lgru_tail2:
	ds_read_b128 v[190:193], v156 offset:0
	ds_read_b128 v[194:197], v156 offset:1024
	ds_read_b128 v[198:201], v156 offset:2048
	ds_read_b128 v[202:205], v156 offset:3072
	v_exp_f32_e32 v228, v144
	v_exp_f32_e32 v229, v145
	v_exp_f32_e32 v230, v146
	v_exp_f32_e32 v231, v147
	v_exp_f32_e32 v232, v148
	v_exp_f32_e32 v233, v149
	v_exp_f32_e32 v234, v150
	v_exp_f32_e32 v235, v151
	v_add_f32_e32 v228, 1.0, v228
	v_add_f32_e32 v229, 1.0, v229
	v_add_f32_e32 v230, 1.0, v230
	v_add_f32_e32 v231, 1.0, v231
	v_add_f32_e32 v232, 1.0, v232
	v_add_f32_e32 v233, 1.0, v233
	v_add_f32_e32 v234, 1.0, v234
	v_add_f32_e32 v235, 1.0, v235
	v_rcp_f32_e32 v228, v228
	v_rcp_f32_e32 v229, v229
	v_rcp_f32_e32 v230, v230
	v_rcp_f32_e32 v231, v231
	v_fma_f32 v236, v228, v152, v182
	v_fma_f32 v237, v229, v153, v183
	v_fma_f32 v238, v230, v154, v184
	v_fma_f32 v239, v231, v155, v185
	v_exp_f32_e32 v236, v236
	v_exp_f32_e32 v237, v237
	v_exp_f32_e32 v238, v238
	v_exp_f32_e32 v239, v239
	v_rcp_f32_e32 v232, v232
	v_rcp_f32_e32 v233, v233
	v_rcp_f32_e32 v234, v234
	v_rcp_f32_e32 v235, v235
	v_add_f32_e32 v236, 1.0, v236
	v_add_f32_e32 v237, 1.0, v237
	v_add_f32_e32 v238, 1.0, v238
	v_add_f32_e32 v239, 1.0, v239
	v_rcp_f32_e32 v236, v236
	v_rcp_f32_e32 v237, v237
	v_rcp_f32_e32 v238, v238
	v_rcp_f32_e32 v239, v239
	v_pk_fma_f32 v[236:237], v[236:237], -2.0, 1.0 op_sel_hi:[1,0,0]
	v_pk_fma_f32 v[238:239], v[238:239], -2.0, 1.0 op_sel_hi:[1,0,0]
	v_pk_add_f32 v[240:241], v[168:169], v[236:237] neg_lo:[0,1] neg_hi:[0,1]
	v_pk_add_f32 v[242:243], v[170:171], v[238:239] neg_lo:[0,1] neg_hi:[0,1]
	v_pk_fma_f32 v[168:169], v[232:233], v[240:241], v[236:237]
	v_pk_fma_f32 v[170:171], v[234:235], v[242:243], v[238:239]
	v_cvt_pk_f16_f32 v244, v168, v169
	v_cvt_pk_f16_f32 v245, v170, v171
	ds_write_b64 v163, v[244:245] offset:4096
	s_waitcnt lgkmcnt(1)
	v_mfma_f32_16x16x32_f16 v[96:99], v[72:75], v[190:193], v[96:99]
	v_mfma_f32_16x16x32_f16 v[96:99], v[8:11], v[194:197], v[96:99]
	v_mfma_f32_16x16x32_f16 v[96:99], v[4:7], v[198:201], v[96:99]
	v_mfma_f32_16x16x32_f16 v[96:99], v[0:3], v[202:205], v[96:99]
	s_waitcnt lgkmcnt(0)
	s_barrier
	ds_read_b128 v[206:209], v156 offset:4096
	ds_read_b128 v[210:213], v156 offset:5120
	ds_read_b128 v[214:217], v156 offset:6144
	ds_read_b128 v[218:221], v156 offset:7168
	s_lshl_b32 s0, s16, 21
	s_add_u32 s4, s10, s0
	s_addc_u32 s5, s11, 0
	s_lshl_b64 s[0:1], s[2:3], 9
	s_add_u32 s0, s4, s0
	s_addc_u32 s1, s5, s1
	v_lshlrev_b32_e32 v222, 9, v161
	v_mov_b32_e32 v223, 0
	v_lshlrev_b32_e32 v224, 2, v162
	v_mov_b32_e32 v225, 0
	v_lshl_add_u64 v[186:187], s[0:1], 0, v[224:225]
	v_lshlrev_b32_e32 v224, 2, v160
	v_lshl_add_u64 v[186:187], v[186:187], 0, v[224:225]
	v_lshl_add_u64 v[188:189], v[186:187], 0, v[222:223]
	v_or_b32_e32 v222, 0x2000, v222
	v_lshl_add_u64 v[246:247], v[186:187], 0, v[222:223]
	s_waitcnt lgkmcnt(0)
	v_mfma_f32_16x16x32_f16 v[92:95], v[72:75], v[206:209], v[92:95]
	v_mfma_f32_16x16x32_f16 v[92:95], v[8:11], v[210:213], v[92:95]
	v_mfma_f32_16x16x32_f16 v[92:95], v[4:7], v[214:217], v[92:95]
	v_mfma_f32_16x16x32_f16 v[92:95], v[0:3], v[218:221], v[92:95]
	s_nop 7
	s_nop 3
	global_store_dwordx4 v[188:189], v[96:99], off
	global_store_dwordx4 v[246:247], v[92:95], off
	s_endpgm

	.amdhsa_kernel _Z10gru_kernelPKhPf
		.amdhsa_group_segment_fixed_size 125728
		.amdhsa_private_segment_fixed_size 0
		.amdhsa_kernarg_size 16
		.amdhsa_user_sgpr_count 2
		.amdhsa_user_sgpr_dispatch_ptr 0
		.amdhsa_user_sgpr_queue_ptr 0
		.amdhsa_user_sgpr_kernarg_segment_ptr 1
		.amdhsa_user_sgpr_dispatch_id 0
		.amdhsa_user_sgpr_kernarg_preload_length 0
		.amdhsa_user_sgpr_kernarg_preload_offset 0
		.amdhsa_user_sgpr_private_segment_size 0
		.amdhsa_uses_dynamic_stack 0
		.amdhsa_enable_private_segment 0
		.amdhsa_system_sgpr_workgroup_id_x 1
		.amdhsa_system_sgpr_workgroup_id_y 0
		.amdhsa_system_sgpr_workgroup_id_z 0
		.amdhsa_system_sgpr_workgroup_info 0
		.amdhsa_system_vgpr_workitem_id 0
		.amdhsa_next_free_vgpr 248
		.amdhsa_next_free_sgpr 19
		.amdhsa_accum_offset 248
		.amdhsa_reserve_vcc 1
		.amdhsa_float_round_mode_32 0
		.amdhsa_float_round_mode_16_64 0
		.amdhsa_float_denorm_mode_32 3
		.amdhsa_float_denorm_mode_16_64 3
		.amdhsa_dx10_clamp 1
		.amdhsa_ieee_mode 1
		.amdhsa_fp16_overflow 0
		.amdhsa_tg_split 0
		.amdhsa_exception_fp_ieee_invalid_op 0
		.amdhsa_exception_fp_denorm_src 0
		.amdhsa_exception_fp_ieee_div_zero 0
		.amdhsa_exception_fp_ieee_overflow 0
		.amdhsa_exception_fp_ieee_underflow 0
		.amdhsa_exception_fp_ieee_inexact 0
		.amdhsa_exception_int_div_zero 0
	.end_amdhsa_kernel

.Lfunc_end1:
	.size	_Z10gru_kernelPKhPf, .Lfunc_end1-_Z10gru_kernelPKhPf
	.set _Z10gru_kernelPKhPf.num_vgpr, 248
	.set _Z10gru_kernelPKhPf.num_agpr, 0
	.set _Z10gru_kernelPKhPf.numbered_sgpr, 19
	.set _Z10gru_kernelPKhPf.num_named_barrier, 0
	.set _Z10gru_kernelPKhPf.private_seg_size, 0
	.set _Z10gru_kernelPKhPf.uses_vcc, 1
	.set _Z10gru_kernelPKhPf.uses_flat_scratch, 0
	.set _Z10gru_kernelPKhPf.has_dyn_sized_stack, 0
	.set _Z10gru_kernelPKhPf.has_recursion, 0
	.set _Z10gru_kernelPKhPf.has_indirect_call, 0

amdhsa.kernels:
  - .agpr_count:     0
    .args:
      - .actual_access:  read_only
        .address_space:  global
        .offset:         0
        .size:           8
        .value_kind:     global_buffer
      - .actual_access:  read_only
        .address_space:  global
        .offset:         8
        .size:           8
        .value_kind:     global_buffer
      - .actual_access:  read_only
        .address_space:  global
        .offset:         16
        .size:           8
        .value_kind:     global_buffer
      - .actual_access:  read_only
        .address_space:  global
        .offset:         24
        .size:           8
        .value_kind:     global_buffer
      - .actual_access:  read_only
        .address_space:  global
        .offset:         32
        .size:           8
        .value_kind:     global_buffer
      - .actual_access:  read_only
        .address_space:  global
        .offset:         40
        .size:           8
        .value_kind:     global_buffer
      - .actual_access:  read_only
        .address_space:  global
        .offset:         48
        .size:           8
        .value_kind:     global_buffer
      - .actual_access:  read_only
        .address_space:  global
        .offset:         56
        .size:           8
        .value_kind:     global_buffer
      - .actual_access:  read_only
        .address_space:  global
        .offset:         64
        .size:           8
        .value_kind:     global_buffer
      - .actual_access:  read_only
        .address_space:  global
        .offset:         72
        .size:           8
        .value_kind:     global_buffer
      - .actual_access:  read_only
        .address_space:  global
        .offset:         80
        .size:           8
        .value_kind:     global_buffer
      - .actual_access:  write_only
        .address_space:  global
        .offset:         88
        .size:           8
        .value_kind:     global_buffer
    .group_segment_fixed_size: 512
    .kernarg_segment_align: 8
    .kernarg_segment_size: 96
    .language:       OpenCL C
    .language_version:
      - 2
      - 0
    .max_flat_workgroup_size: 256
    .name:           _Z11prep_kernelPKiS0_PKfS2_S2_S2_S2_S2_S2_S2_S2_Ph
    .private_segment_fixed_size: 0
    .sgpr_count:     22
    .sgpr_spill_count: 0
    .symbol:         _Z11prep_kernelPKiS0_PKfS2_S2_S2_S2_S2_S2_S2_S2_Ph.kd
    .uniform_work_group_size: 1
    .uses_dynamic_stack: false
    .vgpr_count:     16
    .vgpr_spill_count: 0
    .wavefront_size: 64
  - .agpr_count:     0
    .args:
      - .actual_access:  read_only
        .address_space:  global
        .offset:         0
        .size:           8
        .value_kind:     global_buffer
      - .actual_access:  write_only
        .address_space:  global
        .offset:         8
        .size:           8
        .value_kind:     global_buffer
    .group_segment_fixed_size: 125728
    .kernarg_segment_align: 8
    .kernarg_segment_size: 16
    .language:       OpenCL C
    .language_version:
      - 2
      - 0
    .max_flat_workgroup_size: 512
    .name:           _Z10gru_kernelPKhPf
    .private_segment_fixed_size: 0
    .sgpr_count:     25
    .sgpr_spill_count: 0
    .symbol:         _Z10gru_kernelPKhPf.kd
    .uniform_work_group_size: 1
    .uses_dynamic_stack: false
    .vgpr_count:     248
    .vgpr_spill_count: 0
    .wavefront_size: 64
  - .agpr_count:     0
    .args:
      - .actual_access:  read_only
        .address_space:  global
        .offset:         0
        .size:           8
        .value_kind:     global_buffer
      - .actual_access:  read_only
        .address_space:  global
        .offset:         8
        .size:           8
        .value_kind:     global_buffer
      - .actual_access:  write_only
        .address_space:  global
        .offset:         16
        .size:           8
        .value_kind:     global_buffer
    .group_segment_fixed_size: 0
    .kernarg_segment_align: 8
    .kernarg_segment_size: 24
    .language:       OpenCL C
    .language_version:
      - 2
      - 0
    .max_flat_workgroup_size: 256
    .name:           _Z12final_kernelPKfS0_Pf
    .private_segment_fixed_size: 0
    .sgpr_count:     16
    .sgpr_spill_count: 0
    .symbol:         _Z12final_kernelPKfS0_Pf.kd
    .uniform_work_group_size: 1
    .uses_dynamic_stack: false
    .vgpr_count:     26
    .vgpr_spill_count: 0
    .wavefront_size: 64
